# QKV GEMM epilogue: the 64 bf16 output stores (4 layers x 16) carry sc1 so the written lines are not kept in the writer XCD L2 (operand tiles keep the L2)
# speedup vs baseline: 1.0022x; 1.0022x over previous
.LBB0_239:
	s_lshl_b32 s13, s1, 8
	v_readlane_b32 s40, v254, 46
	v_or_b32_e32 v4, s13, v187
	s_cmpk_lt_i32 s13, 0x400
	v_readlane_b32 s41, v254, 47
	s_cselect_b64 vcc, -1, 0
	v_lshl_add_u32 v1, s0, 8, v182
	v_ashrrev_i32_e32 v5, 31, v4
	v_mov_b64_e32 v[2:3], s[40:41]
	v_cndmask_b32_e32 v0, v204, v205, vcc
	v_mad_i64_i32 v[6:7], s[40:41], v1, s53, v[2:3]
	v_lshlrev_b64 v[4:5], 1, v[4:5]
	v_lshl_add_u64 v[10:11], v[6:7], 0, v[4:5]
	v_pk_mul_f32 v[6:7], v[0:1], v[156:157] op_sel_hi:[0,1]
	v_pk_mul_f32 v[8:9], v[0:1], v[158:159] op_sel_hi:[0,1]
	v_cvt_pk_bf16_f32 v6, v6, v7
	v_cvt_pk_bf16_f32 v7, v8, v9
	v_pk_mul_f32 v[12:13], v[0:1], v[126:127] op_sel_hi:[0,1]
	v_pk_mul_f32 v[14:15], v[0:1], v[124:125] op_sel_hi:[0,1]
	v_cvt_pk_bf16_f32 v8, v14, v15
	v_cvt_pk_bf16_f32 v9, v12, v13
	global_store_dwordx4 v[10:11], v[6:9], off sc1
	v_pk_mul_f32 v[12:13], v[0:1], v[46:47] op_sel_hi:[0,1]
	v_pk_mul_f32 v[14:15], v[0:1], v[44:45] op_sel_hi:[0,1]
	v_pk_mul_f32 v[6:7], v[0:1], v[72:73] op_sel_hi:[0,1]
	v_pk_mul_f32 v[8:9], v[0:1], v[74:75] op_sel_hi:[0,1]
	v_cvt_pk_bf16_f32 v6, v6, v7
	v_cvt_pk_bf16_f32 v7, v8, v9
	v_cvt_pk_bf16_f32 v8, v14, v15
	v_cvt_pk_bf16_f32 v9, v12, v13
	global_store_dwordx4 v[10:11], v[6:9], off offset:256 sc1
	v_pk_mul_f32 v[12:13], v[0:1], v[114:115] op_sel_hi:[0,1]
	v_pk_mul_f32 v[14:15], v[0:1], v[112:113] op_sel_hi:[0,1]
	v_or_b32_e32 v6, 16, v1
	v_mad_i64_i32 v[6:7], s[40:41], v6, s53, v[2:3]
	v_lshl_add_u64 v[10:11], v[6:7], 0, v[4:5]
	v_pk_mul_f32 v[6:7], v[0:1], v[144:145] op_sel_hi:[0,1]
	v_pk_mul_f32 v[8:9], v[0:1], v[146:147] op_sel_hi:[0,1]
	v_cvt_pk_bf16_f32 v6, v6, v7
	v_cvt_pk_bf16_f32 v7, v8, v9
	v_cvt_pk_bf16_f32 v8, v14, v15
	v_cvt_pk_bf16_f32 v9, v12, v13
	global_store_dwordx4 v[10:11], v[6:9], off sc1
	v_pk_mul_f32 v[12:13], v[0:1], v[42:43] op_sel_hi:[0,1]
	v_pk_mul_f32 v[14:15], v[0:1], v[40:41] op_sel_hi:[0,1]
	v_pk_mul_f32 v[6:7], v[0:1], v[56:57] op_sel_hi:[0,1]
	v_pk_mul_f32 v[8:9], v[0:1], v[58:59] op_sel_hi:[0,1]
	v_cvt_pk_bf16_f32 v6, v6, v7
	v_cvt_pk_bf16_f32 v7, v8, v9
	v_cvt_pk_bf16_f32 v8, v14, v15
	v_cvt_pk_bf16_f32 v9, v12, v13
	global_store_dwordx4 v[10:11], v[6:9], off offset:256 sc1
	v_pk_mul_f32 v[12:13], v[0:1], v[110:111] op_sel_hi:[0,1]
	v_pk_mul_f32 v[14:15], v[0:1], v[108:109] op_sel_hi:[0,1]
	v_or_b32_e32 v6, 32, v1
	v_mad_i64_i32 v[6:7], s[40:41], v6, s53, v[2:3]
	v_lshl_add_u64 v[10:11], v[6:7], 0, v[4:5]
	v_pk_mul_f32 v[6:7], v[0:1], v[140:141] op_sel_hi:[0,1]
	v_pk_mul_f32 v[8:9], v[0:1], v[142:143] op_sel_hi:[0,1]
	v_cvt_pk_bf16_f32 v6, v6, v7
	v_cvt_pk_bf16_f32 v7, v8, v9
	v_cvt_pk_bf16_f32 v8, v14, v15
	v_cvt_pk_bf16_f32 v9, v12, v13
	global_store_dwordx4 v[10:11], v[6:9], off sc1
	v_pk_mul_f32 v[12:13], v[0:1], v[38:39] op_sel_hi:[0,1]
	v_pk_mul_f32 v[14:15], v[0:1], v[36:37] op_sel_hi:[0,1]
	v_pk_mul_f32 v[6:7], v[0:1], v[52:53] op_sel_hi:[0,1]
	v_pk_mul_f32 v[8:9], v[0:1], v[54:55] op_sel_hi:[0,1]
	v_cvt_pk_bf16_f32 v6, v6, v7
	v_cvt_pk_bf16_f32 v7, v8, v9
	v_cvt_pk_bf16_f32 v8, v14, v15
	v_cvt_pk_bf16_f32 v9, v12, v13
	global_store_dwordx4 v[10:11], v[6:9], off offset:256 sc1
	v_pk_mul_f32 v[12:13], v[0:1], v[98:99] op_sel_hi:[0,1]
	v_pk_mul_f32 v[14:15], v[0:1], v[96:97] op_sel_hi:[0,1]
	v_or_b32_e32 v6, 48, v1
	v_mad_i64_i32 v[6:7], s[40:41], v6, s53, v[2:3]
	v_lshl_add_u64 v[10:11], v[6:7], 0, v[4:5]
	v_pk_mul_f32 v[6:7], v[0:1], v[136:137] op_sel_hi:[0,1]
	v_pk_mul_f32 v[8:9], v[0:1], v[138:139] op_sel_hi:[0,1]
	v_cvt_pk_bf16_f32 v6, v6, v7
	v_cvt_pk_bf16_f32 v7, v8, v9
	v_cvt_pk_bf16_f32 v8, v14, v15
	v_cvt_pk_bf16_f32 v9, v12, v13
	global_store_dwordx4 v[10:11], v[6:9], off sc1
	v_pk_mul_f32 v[12:13], v[0:1], v[34:35] op_sel_hi:[0,1]
	v_pk_mul_f32 v[14:15], v[0:1], v[32:33] op_sel_hi:[0,1]
	v_pk_mul_f32 v[6:7], v[0:1], v[48:49] op_sel_hi:[0,1]
	v_pk_mul_f32 v[8:9], v[0:1], v[50:51] op_sel_hi:[0,1]
	v_cvt_pk_bf16_f32 v6, v6, v7
	v_cvt_pk_bf16_f32 v7, v8, v9
	v_cvt_pk_bf16_f32 v8, v14, v15
	v_cvt_pk_bf16_f32 v9, v12, v13
	global_store_dwordx4 v[10:11], v[6:9], off offset:256 sc1
	v_pk_mul_f32 v[12:13], v[0:1], v[86:87] op_sel_hi:[0,1]
	v_pk_mul_f32 v[14:15], v[0:1], v[84:85] op_sel_hi:[0,1]
	v_add_u32_e32 v6, 0x80, v1
	v_mad_i64_i32 v[6:7], s[40:41], v6, s53, v[2:3]
	v_lshl_add_u64 v[10:11], v[6:7], 0, v[4:5]
	v_pk_mul_f32 v[6:7], v[0:1], v[128:129] op_sel_hi:[0,1]
	v_pk_mul_f32 v[8:9], v[0:1], v[130:131] op_sel_hi:[0,1]
	v_cvt_pk_bf16_f32 v6, v6, v7
	v_cvt_pk_bf16_f32 v7, v8, v9
	v_cvt_pk_bf16_f32 v8, v14, v15
	v_cvt_pk_bf16_f32 v9, v12, v13
	global_store_dwordx4 v[10:11], v[6:9], off sc1
	v_pk_mul_f32 v[12:13], v[0:1], v[62:63] op_sel_hi:[0,1]
	v_pk_mul_f32 v[14:15], v[0:1], v[60:61] op_sel_hi:[0,1]
	v_pk_mul_f32 v[6:7], v[0:1], v[88:89] op_sel_hi:[0,1]
	v_pk_mul_f32 v[8:9], v[0:1], v[90:91] op_sel_hi:[0,1]
	v_cvt_pk_bf16_f32 v6, v6, v7
	v_cvt_pk_bf16_f32 v7, v8, v9
	v_cvt_pk_bf16_f32 v8, v14, v15
	v_cvt_pk_bf16_f32 v9, v12, v13
	global_store_dwordx4 v[10:11], v[6:9], off offset:256 sc1
	v_pk_mul_f32 v[12:13], v[0:1], v[66:67] op_sel_hi:[0,1]
	v_pk_mul_f32 v[14:15], v[0:1], v[64:65] op_sel_hi:[0,1]
	v_add_u32_e32 v6, 0x90, v1
	v_mad_i64_i32 v[6:7], s[40:41], v6, s53, v[2:3]
	v_lshl_add_u64 v[10:11], v[6:7], 0, v[4:5]
	v_pk_mul_f32 v[6:7], v[0:1], v[116:117] op_sel_hi:[0,1]
	v_pk_mul_f32 v[8:9], v[0:1], v[118:119] op_sel_hi:[0,1]
	v_cvt_pk_bf16_f32 v6, v6, v7
	v_cvt_pk_bf16_f32 v7, v8, v9
	v_cvt_pk_bf16_f32 v8, v14, v15
	v_cvt_pk_bf16_f32 v9, v12, v13
	global_store_dwordx4 v[10:11], v[6:9], off sc1
	v_pk_mul_f32 v[12:13], v[0:1], v[70:71] op_sel_hi:[0,1]
	v_pk_mul_f32 v[14:15], v[0:1], v[68:69] op_sel_hi:[0,1]
	v_pk_mul_f32 v[6:7], v[0:1], v[92:93] op_sel_hi:[0,1]
	v_pk_mul_f32 v[8:9], v[0:1], v[94:95] op_sel_hi:[0,1]
	v_cvt_pk_bf16_f32 v6, v6, v7
	v_cvt_pk_bf16_f32 v7, v8, v9
	v_cvt_pk_bf16_f32 v8, v14, v15
	v_cvt_pk_bf16_f32 v9, v12, v13
	global_store_dwordx4 v[10:11], v[6:9], off offset:256 sc1
	v_pk_mul_f32 v[12:13], v[0:1], v[122:123] op_sel_hi:[0,1]
	v_pk_mul_f32 v[14:15], v[0:1], v[120:121] op_sel_hi:[0,1]
	v_add_u32_e32 v6, 0xa0, v1
	v_mad_i64_i32 v[6:7], s[40:41], v6, s53, v[2:3]
	v_lshl_add_u64 v[10:11], v[6:7], 0, v[4:5]
	v_pk_mul_f32 v[8:9], v[0:1], v[150:151] op_sel_hi:[0,1]
	v_pk_mul_f32 v[6:7], v[0:1], v[148:149] op_sel_hi:[0,1]
	v_cvt_pk_bf16_f32 v6, v6, v7
	v_cvt_pk_bf16_f32 v7, v8, v9
	v_cvt_pk_bf16_f32 v8, v14, v15
	v_cvt_pk_bf16_f32 v9, v12, v13
	global_store_dwordx4 v[10:11], v[6:9], off sc1
	v_pk_mul_f32 v[12:13], v[0:1], v[78:79] op_sel_hi:[0,1]
	v_pk_mul_f32 v[14:15], v[0:1], v[76:77] op_sel_hi:[0,1]
	v_pk_mul_f32 v[8:9], v[0:1], v[102:103] op_sel_hi:[0,1]
	v_pk_mul_f32 v[6:7], v[0:1], v[100:101] op_sel_hi:[0,1]
	v_add_u32_e32 v1, 0xb0, v1
	v_cvt_pk_bf16_f32 v6, v6, v7
	v_cvt_pk_bf16_f32 v7, v8, v9
	v_mad_i64_i32 v[2:3], s[40:41], v1, s53, v[2:3]
	v_cvt_pk_bf16_f32 v8, v14, v15
	v_cvt_pk_bf16_f32 v9, v12, v13
	global_store_dwordx4 v[10:11], v[6:9], off offset:256 sc1
	s_and_b32 s1, s1, -4
	v_pk_mul_f32 v[10:11], v[0:1], v[132:133] op_sel_hi:[0,1]
	v_lshl_add_u64 v[6:7], v[2:3], 0, v[4:5]
	v_pk_mul_f32 v[2:3], v[0:1], v[152:153] op_sel_hi:[0,1]
	v_pk_mul_f32 v[4:5], v[0:1], v[154:155] op_sel_hi:[0,1]
	v_cvt_pk_bf16_f32 v2, v2, v3
	v_cvt_pk_bf16_f32 v3, v4, v5
	v_pk_mul_f32 v[8:9], v[0:1], v[134:135] op_sel_hi:[0,1]
	v_cvt_pk_bf16_f32 v4, v10, v11
	v_cvt_pk_bf16_f32 v5, v8, v9
	global_store_dwordx4 v[6:7], v[2:5], off sc1
	s_cmp_lg_u32 s1, 4
	v_pk_mul_f32 v[8:9], v[0:1], v[82:83] op_sel_hi:[0,1]
	v_pk_mul_f32 v[2:3], v[0:1], v[106:107] op_sel_hi:[0,1]
	v_pk_mul_f32 v[4:5], v[0:1], v[104:105] op_sel_hi:[0,1]
	v_pk_mul_f32 v[10:11], v[0:1], v[80:81] op_sel_hi:[0,1]
	v_cvt_pk_bf16_f32 v0, v4, v5
	v_cvt_pk_bf16_f32 v1, v2, v3
	v_cvt_pk_bf16_f32 v2, v10, v11
	v_cvt_pk_bf16_f32 v3, v8, v9
	global_store_dwordx4 v[6:7], v[0:3], off offset:256 sc1
	s_cbranch_scc1 .LBB0_243
	s_nop 0
	v_pk_add_f32 v[2:3], v[156:157], 0 op_sel_hi:[1,0]
	v_and_b32_e32 v0, 64, v206
	v_pk_add_f32 v[2:3], v[2:3], v[144:145]
	v_add_u32_e32 v4, 64, v0
	v_pk_add_f32 v[2:3], v[2:3], v[140:141]
	v_pk_add_f32 v[0:1], v[158:159], 0 op_sel_hi:[1,0]
	v_pk_add_f32 v[2:3], v[2:3], v[136:137]
	v_pk_add_f32 v[0:1], v[0:1], v[146:147]
	v_pk_add_f32 v[2:3], v[2:3], v[128:129]
	v_xor_b32_e32 v5, 1, v206
	v_pk_add_f32 v[0:1], v[0:1], v[142:143]
	v_pk_add_f32 v[2:3], v[2:3], v[116:117]
	v_cmp_lt_i32_e32 vcc, v5, v4
	v_pk_add_f32 v[0:1], v[0:1], v[138:139]
	v_pk_add_f32 v[2:3], v[2:3], v[148:149]
	v_cndmask_b32_e32 v5, v206, v5, vcc
	v_pk_add_f32 v[0:1], v[0:1], v[130:131]
	v_pk_add_f32 v[2:3], v[2:3], v[152:153]
	v_lshlrev_b32_e32 v21, 2, v5
	v_pk_add_f32 v[0:1], v[0:1], v[118:119]
	ds_bpermute_b32 v5, v21, v2
	v_pk_add_f32 v[0:1], v[0:1], v[150:151]
	ds_bpermute_b32 v6, v21, v3
	v_pk_add_f32 v[0:1], v[0:1], v[154:155]
	ds_bpermute_b32 v7, v21, v0
	s_waitcnt lgkmcnt(0)
	v_add_f32_e32 v2, v2, v5
	v_xor_b32_e32 v5, 2, v206
	ds_bpermute_b32 v8, v21, v1
	v_cmp_lt_i32_e32 vcc, v5, v4
	v_add_f32_e32 v0, v0, v7
	v_add_f32_e32 v3, v3, v6
	v_cndmask_b32_e32 v5, v206, v5, vcc
	v_lshlrev_b32_e32 v26, 2, v5
	ds_bpermute_b32 v5, v26, v2
	ds_bpermute_b32 v7, v26, v0
	s_waitcnt lgkmcnt(0)
	v_add_f32_e32 v1, v1, v8
	ds_bpermute_b32 v6, v26, v3
	ds_bpermute_b32 v8, v26, v1
	v_add_f32_e32 v2, v2, v5
	v_add_f32_e32 v5, v0, v7
	v_xor_b32_e32 v0, 4, v206
	v_cmp_lt_i32_e32 vcc, v0, v4
	s_waitcnt lgkmcnt(0)
	v_add_f32_e32 v3, v3, v6
	v_add_f32_e32 v6, v1, v8
	v_cndmask_b32_e32 v0, v206, v0, vcc
	v_lshlrev_b32_e32 v27, 2, v0
	ds_bpermute_b32 v0, v27, v2
	ds_bpermute_b32 v1, v27, v3
	ds_bpermute_b32 v7, v27, v5
	ds_bpermute_b32 v8, v27, v6
	v_pk_add_f32 v[16:17], v[72:73], 0 op_sel_hi:[1,0]
	s_waitcnt lgkmcnt(0)
	v_add_f32_e32 v0, v2, v0
	v_add_f32_e32 v1, v3, v1
	v_add_f32_e32 v2, v5, v7
	v_add_f32_e32 v3, v6, v8
	v_pk_add_f32 v[6:7], v[126:127], 0 op_sel_hi:[1,0]
	v_pk_add_f32 v[8:9], v[124:125], 0 op_sel_hi:[1,0]
	v_pk_add_f32 v[6:7], v[6:7], v[114:115]
	v_pk_add_f32 v[8:9], v[8:9], v[112:113]
	v_pk_add_f32 v[6:7], v[6:7], v[110:111]
	v_pk_add_f32 v[8:9], v[8:9], v[108:109]
	v_pk_add_f32 v[6:7], v[6:7], v[98:99]
	v_pk_add_f32 v[8:9], v[8:9], v[96:97]
	v_pk_add_f32 v[6:7], v[6:7], v[86:87]
	v_pk_add_f32 v[8:9], v[8:9], v[84:85]
	v_pk_add_f32 v[6:7], v[6:7], v[66:67]
	v_pk_add_f32 v[8:9], v[8:9], v[64:65]
	v_pk_add_f32 v[6:7], v[6:7], v[122:123]
	v_pk_add_f32 v[8:9], v[8:9], v[120:121]
	v_pk_add_f32 v[6:7], v[6:7], v[134:135]
	v_pk_add_f32 v[8:9], v[8:9], v[132:133]
	ds_bpermute_b32 v10, v21, v8
	ds_bpermute_b32 v12, v21, v6
	ds_bpermute_b32 v13, v21, v7
	ds_bpermute_b32 v11, v21, v9
	v_pk_add_f32 v[16:17], v[16:17], v[56:57]
	s_waitcnt lgkmcnt(0)
	v_add_f32_e32 v8, v8, v10
	v_add_f32_e32 v10, v6, v12
	v_add_f32_e32 v7, v7, v13
	v_add_f32_e32 v9, v9, v11
	ds_bpermute_b32 v11, v26, v8
	ds_bpermute_b32 v13, v26, v10
	ds_bpermute_b32 v14, v26, v7
	ds_bpermute_b32 v12, v26, v9
	v_pk_add_f32 v[16:17], v[16:17], v[52:53]
	s_waitcnt lgkmcnt(0)
	v_add_f32_e32 v8, v8, v11
	v_add_f32_e32 v10, v10, v13
	v_add_f32_e32 v11, v7, v14
	v_add_f32_e32 v9, v9, v12
	ds_bpermute_b32 v12, v27, v8
	ds_bpermute_b32 v14, v27, v10
	ds_bpermute_b32 v15, v27, v11
	v_pk_add_f32 v[16:17], v[16:17], v[48:49]
	ds_bpermute_b32 v13, v27, v9
	s_waitcnt lgkmcnt(0)
	v_add_f32_e32 v8, v8, v12
	v_add_f32_e32 v10, v10, v14
	v_add_f32_e32 v12, v11, v15
	v_pk_add_f32 v[14:15], v[74:75], 0 op_sel_hi:[1,0]
	v_pk_add_f32 v[16:17], v[16:17], v[88:89]
	v_pk_add_f32 v[14:15], v[14:15], v[58:59]
	v_pk_add_f32 v[16:17], v[16:17], v[92:93]
	v_pk_add_f32 v[14:15], v[14:15], v[54:55]
	v_pk_add_f32 v[16:17], v[16:17], v[100:101]
	v_pk_add_f32 v[14:15], v[14:15], v[50:51]
	v_pk_add_f32 v[16:17], v[16:17], v[104:105]
	v_pk_add_f32 v[14:15], v[14:15], v[90:91]
	ds_bpermute_b32 v18, v21, v16
	v_pk_add_f32 v[14:15], v[14:15], v[94:95]
	ds_bpermute_b32 v19, v21, v17
	v_pk_add_f32 v[14:15], v[14:15], v[102:103]
	v_xor_b32_e32 v5, 8, v206
	v_pk_add_f32 v[14:15], v[14:15], v[106:107]
	ds_bpermute_b32 v20, v21, v14
	ds_bpermute_b32 v22, v21, v15
	s_waitcnt lgkmcnt(0)
	v_add_f32_e32 v16, v16, v18
	v_add_f32_e32 v17, v17, v19
	ds_bpermute_b32 v19, v26, v16
	v_add_f32_e32 v18, v14, v20
	v_add_f32_e32 v15, v15, v22
	ds_bpermute_b32 v20, v26, v17
	ds_bpermute_b32 v22, v26, v18
	ds_bpermute_b32 v23, v26, v15
	s_waitcnt lgkmcnt(0)
	v_add_f32_e32 v16, v16, v19
	v_cmp_lt_i32_e32 vcc, v5, v4
	v_add_f32_e32 v17, v17, v20
	v_add_f32_e32 v18, v18, v22
	v_add_f32_e32 v19, v15, v23
	ds_bpermute_b32 v20, v27, v16
	ds_bpermute_b32 v22, v27, v17
	ds_bpermute_b32 v23, v27, v18
	ds_bpermute_b32 v24, v27, v19
	v_cndmask_b32_e32 v4, v206, v5, vcc
	s_waitcnt lgkmcnt(0)
	v_add_f32_e32 v16, v16, v20
	v_add_f32_e32 v17, v17, v22
	v_add_f32_e32 v18, v18, v23
	v_add_f32_e32 v20, v19, v24
	v_pk_add_f32 v[22:23], v[46:47], 0 op_sel_hi:[1,0]
	v_pk_add_f32 v[24:25], v[44:45], 0 op_sel_hi:[1,0]
	v_pk_add_f32 v[22:23], v[22:23], v[42:43]
	v_pk_add_f32 v[24:25], v[24:25], v[40:41]
	v_pk_add_f32 v[22:23], v[22:23], v[38:39]
	v_pk_add_f32 v[24:25], v[24:25], v[36:37]
	v_pk_add_f32 v[22:23], v[22:23], v[34:35]
	v_pk_add_f32 v[24:25], v[24:25], v[32:33]
	v_pk_add_f32 v[22:23], v[22:23], v[62:63]
	v_pk_add_f32 v[24:25], v[24:25], v[60:61]
	v_pk_add_f32 v[22:23], v[22:23], v[70:71]
	v_pk_add_f32 v[24:25], v[24:25], v[68:69]
	v_pk_add_f32 v[22:23], v[22:23], v[78:79]
	v_pk_add_f32 v[24:25], v[24:25], v[76:77]
	v_pk_add_f32 v[22:23], v[22:23], v[82:83]
	v_pk_add_f32 v[24:25], v[24:25], v[80:81]
	ds_bpermute_b32 v28, v21, v24
	ds_bpermute_b32 v29, v21, v25
	ds_bpermute_b32 v30, v21, v22
	ds_bpermute_b32 v32, v21, v23
	v_lshlrev_b32_e32 v31, 2, v4
	s_waitcnt lgkmcnt(0)
	v_add_f32_e32 v24, v24, v28
	v_add_f32_e32 v25, v25, v29
	v_add_f32_e32 v28, v22, v30
	v_add_f32_e32 v23, v23, v32
	ds_bpermute_b32 v29, v26, v24
	ds_bpermute_b32 v30, v26, v25
	ds_bpermute_b32 v32, v26, v28
	ds_bpermute_b32 v26, v26, v23
	v_add_f32_e32 v9, v9, v13
	s_waitcnt lgkmcnt(0)
	v_add_f32_e32 v24, v24, v29
	v_add_f32_e32 v25, v25, v30
	v_add_f32_e32 v28, v28, v32
	v_add_f32_e32 v29, v23, v26
	ds_bpermute_b32 v26, v27, v24
	ds_bpermute_b32 v30, v27, v25
	ds_bpermute_b32 v32, v27, v28
	ds_bpermute_b32 v27, v27, v29
	ds_bpermute_b32 v4, v31, v0
	s_waitcnt lgkmcnt(0)
	v_add_f32_e32 v24, v24, v26
	v_add_f32_e32 v25, v25, v30
	v_add_f32_e32 v26, v28, v32
	v_add_f32_e32 v28, v29, v27
	ds_bpermute_b32 v5, v31, v1
	ds_bpermute_b32 v6, v31, v2
	ds_bpermute_b32 v7, v31, v3
	ds_bpermute_b32 v11, v31, v8
	ds_bpermute_b32 v13, v31, v9
	ds_bpermute_b32 v14, v31, v10
	ds_bpermute_b32 v15, v31, v12
	ds_bpermute_b32 v19, v31, v16
	ds_bpermute_b32 v21, v31, v17
	ds_bpermute_b32 v22, v31, v18
	ds_bpermute_b32 v23, v31, v20
	ds_bpermute_b32 v27, v31, v24
	ds_bpermute_b32 v29, v31, v25
	ds_bpermute_b32 v30, v31, v26
	ds_bpermute_b32 v31, v31, v28
	s_and_saveexec_b64 s[40:41], s[2:3]
	s_cbranch_execz .LBB0_242
	s_lshl_b32 s1, s0, 1
	s_and_b32 s15, s1, -16
	s_add_i32 s1, s49, s13
	s_lshr_b32 s1, s1, 6
	s_or_b32 s42, s1, s15
	s_ashr_i32 s43, s42, 31
	s_lshl_b64 s[42:43], s[42:43], 11
	s_add_u32 s1, s4, s42
	s_addc_u32 s42, s5, s43
	s_lshl_b32 s0, s0, 8
	s_and_b32 s43, s0, 0x700
	v_add_f32_e32 v0, v0, v4
	s_add_u32 s0, s1, s43
	s_waitcnt lgkmcnt(0)
	v_add_f32_e32 v1, v1, v5
	s_addc_u32 s1, s42, 0
	v_mul_f32_e32 v0, 0x35800000, v0
	v_add_f32_e32 v2, v2, v6
	global_atomic_add_f32 v201, v0, s[0:1]
	v_mul_f32_e32 v0, 0x35800000, v1
	v_add_f32_e32 v3, v3, v7
	global_atomic_add_f32 v201, v0, s[0:1] offset:4
	v_mul_f32_e32 v0, 0x35800000, v2
	global_atomic_add_f32 v201, v0, s[0:1] offset:8
	v_mul_f32_e32 v0, 0x35800000, v3
	global_atomic_add_f32 v201, v0, s[0:1] offset:12
	s_add_i32 s0, s13, s50
	s_lshr_b32 s0, s0, 6
	s_or_b32 s0, s0, s15
	s_ashr_i32 s1, s0, 31
	s_lshl_b64 s[0:1], s[0:1], 11
	s_add_u32 s0, s4, s0
	s_addc_u32 s1, s5, s1
	v_add_f32_e32 v8, v8, v11
	s_add_u32 s0, s0, s43
	v_add_f32_e32 v9, v9, v13
	s_addc_u32 s1, s1, 0
	v_mul_f32_e32 v0, 0x35800000, v8
	v_add_f32_e32 v10, v10, v14
	global_atomic_add_f32 v202, v0, s[0:1]
	v_mul_f32_e32 v0, 0x35800000, v9
	v_add_f32_e32 v12, v12, v15
	global_atomic_add_f32 v201, v0, s[0:1] offset:20
	v_mul_f32_e32 v0, 0x35800000, v10
	global_atomic_add_f32 v202, v0, s[0:1] offset:8
	v_mul_f32_e32 v0, 0x35800000, v12
	global_atomic_add_f32 v201, v0, s[0:1] offset:28
	s_add_i32 s0, s51, s13
	s_lshr_b32 s0, s0, 6
	s_or_b32 s0, s0, s15
	s_ashr_i32 s1, s0, 31
	s_lshl_b64 s[0:1], s[0:1], 11
	s_add_u32 s0, s4, s0
	s_addc_u32 s1, s5, s1
	v_add_f32_e32 v16, v16, v19
	s_add_u32 s0, s0, s43
	v_add_f32_e32 v17, v17, v21
	s_addc_u32 s1, s1, 0
	v_mul_f32_e32 v0, 0x35800000, v16
	v_add_f32_e32 v18, v18, v22
	global_atomic_add_f32 v201, v0, s[0:1]
	v_mul_f32_e32 v0, 0x35800000, v17
	v_add_f32_e32 v20, v20, v23
	global_atomic_add_f32 v201, v0, s[0:1] offset:4
	v_mul_f32_e32 v0, 0x35800000, v18
	global_atomic_add_f32 v201, v0, s[0:1] offset:8
	v_mul_f32_e32 v0, 0x35800000, v20
	s_add_i32 s13, s13, s52
	global_atomic_add_f32 v201, v0, s[0:1] offset:12
	s_lshr_b32 s0, s13, 6
	s_or_b32 s0, s0, s15
	s_ashr_i32 s1, s0, 31
	s_lshl_b64 s[0:1], s[0:1], 11
	s_add_u32 s0, s4, s0
	s_addc_u32 s1, s5, s1
	v_add_f32_e32 v24, v24, v27
	s_add_u32 s0, s0, s43
	v_add_f32_e32 v25, v25, v29
	s_addc_u32 s1, s1, 0
	v_mul_f32_e32 v0, 0x35800000, v24
	v_add_f32_e32 v26, v26, v30
	global_atomic_add_f32 v203, v0, s[0:1]
	v_mul_f32_e32 v0, 0x35800000, v25
	v_add_f32_e32 v28, v28, v31
	global_atomic_add_f32 v201, v0, s[0:1] offset:20
	v_mul_f32_e32 v0, 0x35800000, v26
	global_atomic_add_f32 v203, v0, s[0:1] offset:8
	v_mul_f32_e32 v0, 0x35800000, v28
	global_atomic_add_f32 v201, v0, s[0:1] offset:28

.LBB0_1178:
	s_lshl_b32 s7, s45, 8
	v_readlane_b32 s24, v254, 46
	v_or_b32_e32 v4, s7, v187
	s_cmpk_lt_i32 s7, 0x400
	v_readlane_b32 s25, v254, 47
	s_cselect_b64 vcc, -1, 0
	v_lshl_add_u32 v1, s16, 8, v182
	v_ashrrev_i32_e32 v5, 31, v4
	v_mov_b64_e32 v[2:3], s[24:25]
	v_cndmask_b32_e32 v0, v201, v202, vcc
	v_mad_i64_i32 v[6:7], s[24:25], v1, s44, v[2:3]
	v_lshlrev_b64 v[4:5], 1, v[4:5]
	v_lshl_add_u64 v[10:11], v[6:7], 0, v[4:5]
	v_pk_mul_f32 v[6:7], v[0:1], v[156:157] op_sel_hi:[0,1]
	v_pk_mul_f32 v[8:9], v[0:1], v[158:159] op_sel_hi:[0,1]
	v_cvt_pk_bf16_f32 v6, v6, v7
	v_cvt_pk_bf16_f32 v7, v8, v9
	v_pk_mul_f32 v[12:13], v[0:1], v[154:155] op_sel_hi:[0,1]
	v_pk_mul_f32 v[14:15], v[0:1], v[152:153] op_sel_hi:[0,1]
	v_cvt_pk_bf16_f32 v8, v14, v15
	v_cvt_pk_bf16_f32 v9, v12, v13
	global_store_dwordx4 v[10:11], v[6:9], off sc1
	v_pk_mul_f32 v[12:13], v[0:1], v[142:143] op_sel_hi:[0,1]
	v_pk_mul_f32 v[14:15], v[0:1], v[140:141] op_sel_hi:[0,1]
	v_pk_mul_f32 v[6:7], v[0:1], v[148:149] op_sel_hi:[0,1]
	v_pk_mul_f32 v[8:9], v[0:1], v[150:151] op_sel_hi:[0,1]
	v_cvt_pk_bf16_f32 v6, v6, v7
	v_cvt_pk_bf16_f32 v7, v8, v9
	v_cvt_pk_bf16_f32 v8, v14, v15
	v_cvt_pk_bf16_f32 v9, v12, v13
	global_store_dwordx4 v[10:11], v[6:9], off offset:256 sc1
	v_pk_mul_f32 v[12:13], v[0:1], v[138:139] op_sel_hi:[0,1]
	v_pk_mul_f32 v[14:15], v[0:1], v[136:137] op_sel_hi:[0,1]
	v_or_b32_e32 v6, 16, v1
	v_mad_i64_i32 v[6:7], s[24:25], v6, s44, v[2:3]
	v_lshl_add_u64 v[10:11], v[6:7], 0, v[4:5]
	v_pk_mul_f32 v[6:7], v[0:1], v[144:145] op_sel_hi:[0,1]
	v_pk_mul_f32 v[8:9], v[0:1], v[146:147] op_sel_hi:[0,1]
	v_cvt_pk_bf16_f32 v6, v6, v7
	v_cvt_pk_bf16_f32 v7, v8, v9
	v_cvt_pk_bf16_f32 v8, v14, v15
	v_cvt_pk_bf16_f32 v9, v12, v13
	global_store_dwordx4 v[10:11], v[6:9], off sc1
	v_pk_mul_f32 v[12:13], v[0:1], v[126:127] op_sel_hi:[0,1]
	v_pk_mul_f32 v[14:15], v[0:1], v[124:125] op_sel_hi:[0,1]
	v_pk_mul_f32 v[6:7], v[0:1], v[132:133] op_sel_hi:[0,1]
	v_pk_mul_f32 v[8:9], v[0:1], v[134:135] op_sel_hi:[0,1]
	v_cvt_pk_bf16_f32 v6, v6, v7
	v_cvt_pk_bf16_f32 v7, v8, v9
	v_cvt_pk_bf16_f32 v8, v14, v15
	v_cvt_pk_bf16_f32 v9, v12, v13
	global_store_dwordx4 v[10:11], v[6:9], off offset:256 sc1
	v_pk_mul_f32 v[12:13], v[0:1], v[122:123] op_sel_hi:[0,1]
	v_pk_mul_f32 v[14:15], v[0:1], v[120:121] op_sel_hi:[0,1]
	v_or_b32_e32 v6, 32, v1
	v_mad_i64_i32 v[6:7], s[24:25], v6, s44, v[2:3]
	v_lshl_add_u64 v[10:11], v[6:7], 0, v[4:5]
	v_pk_mul_f32 v[6:7], v[0:1], v[128:129] op_sel_hi:[0,1]
	v_pk_mul_f32 v[8:9], v[0:1], v[130:131] op_sel_hi:[0,1]
	v_cvt_pk_bf16_f32 v6, v6, v7
	v_cvt_pk_bf16_f32 v7, v8, v9
	v_cvt_pk_bf16_f32 v8, v14, v15
	v_cvt_pk_bf16_f32 v9, v12, v13
	global_store_dwordx4 v[10:11], v[6:9], off sc1
	v_pk_mul_f32 v[12:13], v[0:1], v[110:111] op_sel_hi:[0,1]
	v_pk_mul_f32 v[14:15], v[0:1], v[108:109] op_sel_hi:[0,1]
	v_pk_mul_f32 v[6:7], v[0:1], v[116:117] op_sel_hi:[0,1]
	v_pk_mul_f32 v[8:9], v[0:1], v[118:119] op_sel_hi:[0,1]
	v_cvt_pk_bf16_f32 v6, v6, v7
	v_cvt_pk_bf16_f32 v7, v8, v9
	v_cvt_pk_bf16_f32 v8, v14, v15
	v_cvt_pk_bf16_f32 v9, v12, v13
	global_store_dwordx4 v[10:11], v[6:9], off offset:256 sc1
	v_pk_mul_f32 v[12:13], v[0:1], v[106:107] op_sel_hi:[0,1]
	v_pk_mul_f32 v[14:15], v[0:1], v[104:105] op_sel_hi:[0,1]
	v_or_b32_e32 v6, 48, v1
	v_mad_i64_i32 v[6:7], s[24:25], v6, s44, v[2:3]
	v_lshl_add_u64 v[10:11], v[6:7], 0, v[4:5]
	v_pk_mul_f32 v[6:7], v[0:1], v[112:113] op_sel_hi:[0,1]
	v_pk_mul_f32 v[8:9], v[0:1], v[114:115] op_sel_hi:[0,1]
	v_cvt_pk_bf16_f32 v6, v6, v7
	v_cvt_pk_bf16_f32 v7, v8, v9
	v_cvt_pk_bf16_f32 v8, v14, v15
	v_cvt_pk_bf16_f32 v9, v12, v13
	global_store_dwordx4 v[10:11], v[6:9], off sc1
	v_pk_mul_f32 v[12:13], v[0:1], v[90:91] op_sel_hi:[0,1]
	v_pk_mul_f32 v[14:15], v[0:1], v[88:89] op_sel_hi:[0,1]
	v_pk_mul_f32 v[6:7], v[0:1], v[92:93] op_sel_hi:[0,1]
	v_pk_mul_f32 v[8:9], v[0:1], v[94:95] op_sel_hi:[0,1]
	v_cvt_pk_bf16_f32 v6, v6, v7
	v_cvt_pk_bf16_f32 v7, v8, v9
	v_cvt_pk_bf16_f32 v8, v14, v15
	v_cvt_pk_bf16_f32 v9, v12, v13
	global_store_dwordx4 v[10:11], v[6:9], off offset:256 sc1
	v_pk_mul_f32 v[12:13], v[0:1], v[74:75] op_sel_hi:[0,1]
	v_pk_mul_f32 v[14:15], v[0:1], v[72:73] op_sel_hi:[0,1]
	v_add_u32_e32 v6, 0x80, v1
	v_mad_i64_i32 v[6:7], s[24:25], v6, s44, v[2:3]
	v_lshl_add_u64 v[10:11], v[6:7], 0, v[4:5]
	v_pk_mul_f32 v[6:7], v[0:1], v[76:77] op_sel_hi:[0,1]
	v_pk_mul_f32 v[8:9], v[0:1], v[78:79] op_sel_hi:[0,1]
	v_cvt_pk_bf16_f32 v6, v6, v7
	v_cvt_pk_bf16_f32 v7, v8, v9
	v_cvt_pk_bf16_f32 v8, v14, v15
	v_cvt_pk_bf16_f32 v9, v12, v13
	global_store_dwordx4 v[10:11], v[6:9], off sc1
	v_pk_mul_f32 v[12:13], v[0:1], v[98:99] op_sel_hi:[0,1]
	v_pk_mul_f32 v[14:15], v[0:1], v[96:97] op_sel_hi:[0,1]
	v_pk_mul_f32 v[6:7], v[0:1], v[100:101] op_sel_hi:[0,1]
	v_pk_mul_f32 v[8:9], v[0:1], v[102:103] op_sel_hi:[0,1]
	v_cvt_pk_bf16_f32 v6, v6, v7
	v_cvt_pk_bf16_f32 v7, v8, v9
	v_cvt_pk_bf16_f32 v8, v14, v15
	v_cvt_pk_bf16_f32 v9, v12, v13
	global_store_dwordx4 v[10:11], v[6:9], off offset:256 sc1
	v_pk_mul_f32 v[12:13], v[0:1], v[50:51] op_sel_hi:[0,1]
	v_pk_mul_f32 v[14:15], v[0:1], v[48:49] op_sel_hi:[0,1]
	v_add_u32_e32 v6, 0x90, v1
	v_mad_i64_i32 v[6:7], s[24:25], v6, s44, v[2:3]
	v_lshl_add_u64 v[10:11], v[6:7], 0, v[4:5]
	v_pk_mul_f32 v[6:7], v[0:1], v[52:53] op_sel_hi:[0,1]
	v_pk_mul_f32 v[8:9], v[0:1], v[54:55] op_sel_hi:[0,1]
	v_cvt_pk_bf16_f32 v6, v6, v7
	v_cvt_pk_bf16_f32 v7, v8, v9
	v_cvt_pk_bf16_f32 v8, v14, v15
	v_cvt_pk_bf16_f32 v9, v12, v13
	global_store_dwordx4 v[10:11], v[6:9], off sc1
	v_pk_mul_f32 v[12:13], v[0:1], v[82:83] op_sel_hi:[0,1]
	v_pk_mul_f32 v[14:15], v[0:1], v[80:81] op_sel_hi:[0,1]
	v_pk_mul_f32 v[6:7], v[0:1], v[84:85] op_sel_hi:[0,1]
	v_pk_mul_f32 v[8:9], v[0:1], v[86:87] op_sel_hi:[0,1]
	v_cvt_pk_bf16_f32 v6, v6, v7
	v_cvt_pk_bf16_f32 v7, v8, v9
	v_cvt_pk_bf16_f32 v8, v14, v15
	v_cvt_pk_bf16_f32 v9, v12, v13
	global_store_dwordx4 v[10:11], v[6:9], off offset:256 sc1
	v_pk_mul_f32 v[12:13], v[0:1], v[58:59] op_sel_hi:[0,1]
	v_pk_mul_f32 v[14:15], v[0:1], v[56:57] op_sel_hi:[0,1]
	v_add_u32_e32 v6, 0xa0, v1
	v_mad_i64_i32 v[6:7], s[24:25], v6, s44, v[2:3]
	v_lshl_add_u64 v[10:11], v[6:7], 0, v[4:5]
	v_pk_mul_f32 v[8:9], v[0:1], v[62:63] op_sel_hi:[0,1]
	v_pk_mul_f32 v[6:7], v[0:1], v[60:61] op_sel_hi:[0,1]
	v_cvt_pk_bf16_f32 v6, v6, v7
	v_cvt_pk_bf16_f32 v7, v8, v9
	v_cvt_pk_bf16_f32 v8, v14, v15
	v_cvt_pk_bf16_f32 v9, v12, v13
	global_store_dwordx4 v[10:11], v[6:9], off sc1
	v_pk_mul_f32 v[12:13], v[0:1], v[66:67] op_sel_hi:[0,1]
	v_pk_mul_f32 v[14:15], v[0:1], v[64:65] op_sel_hi:[0,1]
	v_pk_mul_f32 v[8:9], v[0:1], v[70:71] op_sel_hi:[0,1]
	v_pk_mul_f32 v[6:7], v[0:1], v[68:69] op_sel_hi:[0,1]
	v_add_u32_e32 v1, 0xb0, v1
	v_cvt_pk_bf16_f32 v6, v6, v7
	v_cvt_pk_bf16_f32 v7, v8, v9
	v_mad_i64_i32 v[2:3], s[24:25], v1, s44, v[2:3]
	v_cvt_pk_bf16_f32 v8, v14, v15
	v_cvt_pk_bf16_f32 v9, v12, v13
	global_store_dwordx4 v[10:11], v[6:9], off offset:256 sc1
	v_pk_mul_f32 v[10:11], v[0:1], v[32:33] op_sel_hi:[0,1]
	s_andn2_b64 vcc, exec, s[10:11]
	v_lshl_add_u64 v[6:7], v[2:3], 0, v[4:5]
	v_pk_mul_f32 v[2:3], v[0:1], v[36:37] op_sel_hi:[0,1]
	v_pk_mul_f32 v[4:5], v[0:1], v[38:39] op_sel_hi:[0,1]
	v_cvt_pk_bf16_f32 v2, v2, v3
	v_cvt_pk_bf16_f32 v3, v4, v5
	v_pk_mul_f32 v[8:9], v[0:1], v[34:35] op_sel_hi:[0,1]
	v_cvt_pk_bf16_f32 v4, v10, v11
	v_cvt_pk_bf16_f32 v5, v8, v9
	global_store_dwordx4 v[6:7], v[2:5], off sc1
	s_mov_b64 s[10:11], -1
	v_pk_mul_f32 v[8:9], v[0:1], v[42:43] op_sel_hi:[0,1]
	v_pk_mul_f32 v[2:3], v[0:1], v[46:47] op_sel_hi:[0,1]
	v_pk_mul_f32 v[4:5], v[0:1], v[44:45] op_sel_hi:[0,1]
	v_pk_mul_f32 v[10:11], v[0:1], v[40:41] op_sel_hi:[0,1]
	v_cvt_pk_bf16_f32 v0, v4, v5
	v_cvt_pk_bf16_f32 v1, v2, v3
	v_cvt_pk_bf16_f32 v2, v10, v11
	v_cvt_pk_bf16_f32 v3, v8, v9
	global_store_dwordx4 v[6:7], v[0:3], off offset:256 sc1
	s_cbranch_vccnz .LBB0_1170
	s_andn2_b64 vcc, exec, s[0:1]
	s_cbranch_vccnz .LBB0_1169
	s_barrier
	s_branch .LBB0_1169

.LBB0_2935:
	s_lshl_b32 s13, s5, 8
	v_readlane_b32 s22, v254, 46
	v_or_b32_e32 v4, s13, v187
	s_cmpk_lt_i32 s13, 0x400
	v_readlane_b32 s23, v254, 47
	s_cselect_b64 vcc, -1, 0
	v_lshl_add_u32 v1, s4, 8, v182
	v_ashrrev_i32_e32 v5, 31, v4
	v_mov_b64_e32 v[2:3], s[22:23]
	v_cndmask_b32_e32 v0, v204, v205, vcc
	v_mad_i64_i32 v[6:7], s[22:23], v1, s53, v[2:3]
	v_lshlrev_b64 v[4:5], 1, v[4:5]
	v_lshl_add_u64 v[10:11], v[6:7], 0, v[4:5]
	v_pk_mul_f32 v[6:7], v[0:1], v[156:157] op_sel_hi:[0,1]
	v_pk_mul_f32 v[8:9], v[0:1], v[158:159] op_sel_hi:[0,1]
	v_cvt_pk_bf16_f32 v6, v6, v7
	v_cvt_pk_bf16_f32 v7, v8, v9
	v_pk_mul_f32 v[12:13], v[0:1], v[126:127] op_sel_hi:[0,1]
	v_pk_mul_f32 v[14:15], v[0:1], v[124:125] op_sel_hi:[0,1]
	v_cvt_pk_bf16_f32 v8, v14, v15
	v_cvt_pk_bf16_f32 v9, v12, v13
	global_store_dwordx4 v[10:11], v[6:9], off sc1
	v_pk_mul_f32 v[12:13], v[0:1], v[46:47] op_sel_hi:[0,1]
	v_pk_mul_f32 v[14:15], v[0:1], v[44:45] op_sel_hi:[0,1]
	v_pk_mul_f32 v[6:7], v[0:1], v[72:73] op_sel_hi:[0,1]
	v_pk_mul_f32 v[8:9], v[0:1], v[74:75] op_sel_hi:[0,1]
	v_cvt_pk_bf16_f32 v6, v6, v7
	v_cvt_pk_bf16_f32 v7, v8, v9
	v_cvt_pk_bf16_f32 v8, v14, v15
	v_cvt_pk_bf16_f32 v9, v12, v13
	global_store_dwordx4 v[10:11], v[6:9], off offset:256 sc1
	v_pk_mul_f32 v[12:13], v[0:1], v[114:115] op_sel_hi:[0,1]
	v_pk_mul_f32 v[14:15], v[0:1], v[112:113] op_sel_hi:[0,1]
	v_or_b32_e32 v6, 16, v1
	v_mad_i64_i32 v[6:7], s[22:23], v6, s53, v[2:3]
	v_lshl_add_u64 v[10:11], v[6:7], 0, v[4:5]
	v_pk_mul_f32 v[6:7], v[0:1], v[144:145] op_sel_hi:[0,1]
	v_pk_mul_f32 v[8:9], v[0:1], v[146:147] op_sel_hi:[0,1]
	v_cvt_pk_bf16_f32 v6, v6, v7
	v_cvt_pk_bf16_f32 v7, v8, v9
	v_cvt_pk_bf16_f32 v8, v14, v15
	v_cvt_pk_bf16_f32 v9, v12, v13
	global_store_dwordx4 v[10:11], v[6:9], off sc1
	v_pk_mul_f32 v[12:13], v[0:1], v[42:43] op_sel_hi:[0,1]
	v_pk_mul_f32 v[14:15], v[0:1], v[40:41] op_sel_hi:[0,1]
	v_pk_mul_f32 v[6:7], v[0:1], v[56:57] op_sel_hi:[0,1]
	v_pk_mul_f32 v[8:9], v[0:1], v[58:59] op_sel_hi:[0,1]
	v_cvt_pk_bf16_f32 v6, v6, v7
	v_cvt_pk_bf16_f32 v7, v8, v9
	v_cvt_pk_bf16_f32 v8, v14, v15
	v_cvt_pk_bf16_f32 v9, v12, v13
	global_store_dwordx4 v[10:11], v[6:9], off offset:256 sc1
	v_pk_mul_f32 v[12:13], v[0:1], v[110:111] op_sel_hi:[0,1]
	v_pk_mul_f32 v[14:15], v[0:1], v[108:109] op_sel_hi:[0,1]
	v_or_b32_e32 v6, 32, v1
	v_mad_i64_i32 v[6:7], s[22:23], v6, s53, v[2:3]
	v_lshl_add_u64 v[10:11], v[6:7], 0, v[4:5]
	v_pk_mul_f32 v[6:7], v[0:1], v[140:141] op_sel_hi:[0,1]
	v_pk_mul_f32 v[8:9], v[0:1], v[142:143] op_sel_hi:[0,1]
	v_cvt_pk_bf16_f32 v6, v6, v7
	v_cvt_pk_bf16_f32 v7, v8, v9
	v_cvt_pk_bf16_f32 v8, v14, v15
	v_cvt_pk_bf16_f32 v9, v12, v13
	global_store_dwordx4 v[10:11], v[6:9], off sc1
	v_pk_mul_f32 v[12:13], v[0:1], v[38:39] op_sel_hi:[0,1]
	v_pk_mul_f32 v[14:15], v[0:1], v[36:37] op_sel_hi:[0,1]
	v_pk_mul_f32 v[6:7], v[0:1], v[52:53] op_sel_hi:[0,1]
	v_pk_mul_f32 v[8:9], v[0:1], v[54:55] op_sel_hi:[0,1]
	v_cvt_pk_bf16_f32 v6, v6, v7
	v_cvt_pk_bf16_f32 v7, v8, v9
	v_cvt_pk_bf16_f32 v8, v14, v15
	v_cvt_pk_bf16_f32 v9, v12, v13
	global_store_dwordx4 v[10:11], v[6:9], off offset:256 sc1
	v_pk_mul_f32 v[12:13], v[0:1], v[98:99] op_sel_hi:[0,1]
	v_pk_mul_f32 v[14:15], v[0:1], v[96:97] op_sel_hi:[0,1]
	v_or_b32_e32 v6, 48, v1
	v_mad_i64_i32 v[6:7], s[22:23], v6, s53, v[2:3]
	v_lshl_add_u64 v[10:11], v[6:7], 0, v[4:5]
	v_pk_mul_f32 v[6:7], v[0:1], v[136:137] op_sel_hi:[0,1]
	v_pk_mul_f32 v[8:9], v[0:1], v[138:139] op_sel_hi:[0,1]
	v_cvt_pk_bf16_f32 v6, v6, v7
	v_cvt_pk_bf16_f32 v7, v8, v9
	v_cvt_pk_bf16_f32 v8, v14, v15
	v_cvt_pk_bf16_f32 v9, v12, v13
	global_store_dwordx4 v[10:11], v[6:9], off sc1
	v_pk_mul_f32 v[12:13], v[0:1], v[34:35] op_sel_hi:[0,1]
	v_pk_mul_f32 v[14:15], v[0:1], v[32:33] op_sel_hi:[0,1]
	v_pk_mul_f32 v[6:7], v[0:1], v[48:49] op_sel_hi:[0,1]
	v_pk_mul_f32 v[8:9], v[0:1], v[50:51] op_sel_hi:[0,1]
	v_cvt_pk_bf16_f32 v6, v6, v7
	v_cvt_pk_bf16_f32 v7, v8, v9
	v_cvt_pk_bf16_f32 v8, v14, v15
	v_cvt_pk_bf16_f32 v9, v12, v13
	global_store_dwordx4 v[10:11], v[6:9], off offset:256 sc1
	v_pk_mul_f32 v[12:13], v[0:1], v[86:87] op_sel_hi:[0,1]
	v_pk_mul_f32 v[14:15], v[0:1], v[84:85] op_sel_hi:[0,1]
	v_add_u32_e32 v6, 0x80, v1
	v_mad_i64_i32 v[6:7], s[22:23], v6, s53, v[2:3]
	v_lshl_add_u64 v[10:11], v[6:7], 0, v[4:5]
	v_pk_mul_f32 v[6:7], v[0:1], v[128:129] op_sel_hi:[0,1]
	v_pk_mul_f32 v[8:9], v[0:1], v[130:131] op_sel_hi:[0,1]
	v_cvt_pk_bf16_f32 v6, v6, v7
	v_cvt_pk_bf16_f32 v7, v8, v9
	v_cvt_pk_bf16_f32 v8, v14, v15
	v_cvt_pk_bf16_f32 v9, v12, v13
	global_store_dwordx4 v[10:11], v[6:9], off sc1
	v_pk_mul_f32 v[12:13], v[0:1], v[62:63] op_sel_hi:[0,1]
	v_pk_mul_f32 v[14:15], v[0:1], v[60:61] op_sel_hi:[0,1]
	v_pk_mul_f32 v[6:7], v[0:1], v[88:89] op_sel_hi:[0,1]
	v_pk_mul_f32 v[8:9], v[0:1], v[90:91] op_sel_hi:[0,1]
	v_cvt_pk_bf16_f32 v6, v6, v7
	v_cvt_pk_bf16_f32 v7, v8, v9
	v_cvt_pk_bf16_f32 v8, v14, v15
	v_cvt_pk_bf16_f32 v9, v12, v13
	global_store_dwordx4 v[10:11], v[6:9], off offset:256 sc1
	v_pk_mul_f32 v[12:13], v[0:1], v[66:67] op_sel_hi:[0,1]
	v_pk_mul_f32 v[14:15], v[0:1], v[64:65] op_sel_hi:[0,1]
	v_add_u32_e32 v6, 0x90, v1
	v_mad_i64_i32 v[6:7], s[22:23], v6, s53, v[2:3]
	v_lshl_add_u64 v[10:11], v[6:7], 0, v[4:5]
	v_pk_mul_f32 v[6:7], v[0:1], v[116:117] op_sel_hi:[0,1]
	v_pk_mul_f32 v[8:9], v[0:1], v[118:119] op_sel_hi:[0,1]
	v_cvt_pk_bf16_f32 v6, v6, v7
	v_cvt_pk_bf16_f32 v7, v8, v9
	v_cvt_pk_bf16_f32 v8, v14, v15
	v_cvt_pk_bf16_f32 v9, v12, v13
	global_store_dwordx4 v[10:11], v[6:9], off sc1
	v_pk_mul_f32 v[12:13], v[0:1], v[70:71] op_sel_hi:[0,1]
	v_pk_mul_f32 v[14:15], v[0:1], v[68:69] op_sel_hi:[0,1]
	v_pk_mul_f32 v[6:7], v[0:1], v[92:93] op_sel_hi:[0,1]
	v_pk_mul_f32 v[8:9], v[0:1], v[94:95] op_sel_hi:[0,1]
	v_cvt_pk_bf16_f32 v6, v6, v7
	v_cvt_pk_bf16_f32 v7, v8, v9
	v_cvt_pk_bf16_f32 v8, v14, v15
	v_cvt_pk_bf16_f32 v9, v12, v13
	global_store_dwordx4 v[10:11], v[6:9], off offset:256 sc1
	v_pk_mul_f32 v[12:13], v[0:1], v[122:123] op_sel_hi:[0,1]
	v_pk_mul_f32 v[14:15], v[0:1], v[120:121] op_sel_hi:[0,1]
	v_add_u32_e32 v6, 0xa0, v1
	v_mad_i64_i32 v[6:7], s[22:23], v6, s53, v[2:3]
	v_lshl_add_u64 v[10:11], v[6:7], 0, v[4:5]
	v_pk_mul_f32 v[8:9], v[0:1], v[150:151] op_sel_hi:[0,1]
	v_pk_mul_f32 v[6:7], v[0:1], v[148:149] op_sel_hi:[0,1]
	v_cvt_pk_bf16_f32 v6, v6, v7
	v_cvt_pk_bf16_f32 v7, v8, v9
	v_cvt_pk_bf16_f32 v8, v14, v15
	v_cvt_pk_bf16_f32 v9, v12, v13
	global_store_dwordx4 v[10:11], v[6:9], off sc1
	v_pk_mul_f32 v[12:13], v[0:1], v[78:79] op_sel_hi:[0,1]
	v_pk_mul_f32 v[14:15], v[0:1], v[76:77] op_sel_hi:[0,1]
	v_pk_mul_f32 v[8:9], v[0:1], v[102:103] op_sel_hi:[0,1]
	v_pk_mul_f32 v[6:7], v[0:1], v[100:101] op_sel_hi:[0,1]
	v_add_u32_e32 v1, 0xb0, v1
	v_cvt_pk_bf16_f32 v6, v6, v7
	v_cvt_pk_bf16_f32 v7, v8, v9
	v_mad_i64_i32 v[2:3], s[22:23], v1, s53, v[2:3]
	v_cvt_pk_bf16_f32 v8, v14, v15
	v_cvt_pk_bf16_f32 v9, v12, v13
	global_store_dwordx4 v[10:11], v[6:9], off offset:256 sc1
	s_and_b32 s5, s5, -4
	v_pk_mul_f32 v[10:11], v[0:1], v[132:133] op_sel_hi:[0,1]
	v_lshl_add_u64 v[6:7], v[2:3], 0, v[4:5]
	v_pk_mul_f32 v[2:3], v[0:1], v[152:153] op_sel_hi:[0,1]
	v_pk_mul_f32 v[4:5], v[0:1], v[154:155] op_sel_hi:[0,1]
	v_cvt_pk_bf16_f32 v2, v2, v3
	v_cvt_pk_bf16_f32 v3, v4, v5
	v_pk_mul_f32 v[8:9], v[0:1], v[134:135] op_sel_hi:[0,1]
	v_cvt_pk_bf16_f32 v4, v10, v11
	v_cvt_pk_bf16_f32 v5, v8, v9
	global_store_dwordx4 v[6:7], v[2:5], off sc1
	s_cmp_lg_u32 s5, 4
	v_pk_mul_f32 v[8:9], v[0:1], v[82:83] op_sel_hi:[0,1]
	v_pk_mul_f32 v[2:3], v[0:1], v[106:107] op_sel_hi:[0,1]
	v_pk_mul_f32 v[4:5], v[0:1], v[104:105] op_sel_hi:[0,1]
	v_pk_mul_f32 v[10:11], v[0:1], v[80:81] op_sel_hi:[0,1]
	v_cvt_pk_bf16_f32 v0, v4, v5
	v_cvt_pk_bf16_f32 v1, v2, v3
	v_cvt_pk_bf16_f32 v2, v10, v11
	v_cvt_pk_bf16_f32 v3, v8, v9
	global_store_dwordx4 v[6:7], v[0:3], off offset:256 sc1
	s_cbranch_scc1 .LBB0_2939
	s_nop 0
	v_pk_add_f32 v[2:3], v[156:157], 0 op_sel_hi:[1,0]
	v_and_b32_e32 v0, 64, v206
	v_pk_add_f32 v[2:3], v[2:3], v[144:145]
	v_add_u32_e32 v4, 64, v0
	v_pk_add_f32 v[2:3], v[2:3], v[140:141]
	v_pk_add_f32 v[0:1], v[158:159], 0 op_sel_hi:[1,0]
	v_pk_add_f32 v[2:3], v[2:3], v[136:137]
	v_pk_add_f32 v[0:1], v[0:1], v[146:147]
	v_pk_add_f32 v[2:3], v[2:3], v[128:129]
	v_xor_b32_e32 v5, 1, v206
	v_pk_add_f32 v[0:1], v[0:1], v[142:143]
	v_pk_add_f32 v[2:3], v[2:3], v[116:117]
	v_cmp_lt_i32_e32 vcc, v5, v4
	v_pk_add_f32 v[0:1], v[0:1], v[138:139]
	v_pk_add_f32 v[2:3], v[2:3], v[148:149]
	v_cndmask_b32_e32 v5, v206, v5, vcc
	v_pk_add_f32 v[0:1], v[0:1], v[130:131]
	v_pk_add_f32 v[2:3], v[2:3], v[152:153]
	v_lshlrev_b32_e32 v21, 2, v5
	v_pk_add_f32 v[0:1], v[0:1], v[118:119]
	ds_bpermute_b32 v5, v21, v2
	v_pk_add_f32 v[0:1], v[0:1], v[150:151]
	ds_bpermute_b32 v6, v21, v3
	v_pk_add_f32 v[0:1], v[0:1], v[154:155]
	ds_bpermute_b32 v7, v21, v0
	s_waitcnt lgkmcnt(0)
	v_add_f32_e32 v2, v2, v5
	v_xor_b32_e32 v5, 2, v206
	ds_bpermute_b32 v8, v21, v1
	v_cmp_lt_i32_e32 vcc, v5, v4
	v_add_f32_e32 v0, v0, v7
	v_add_f32_e32 v3, v3, v6
	v_cndmask_b32_e32 v5, v206, v5, vcc
	v_lshlrev_b32_e32 v26, 2, v5
	ds_bpermute_b32 v5, v26, v2
	ds_bpermute_b32 v7, v26, v0
	s_waitcnt lgkmcnt(0)
	v_add_f32_e32 v1, v1, v8
	ds_bpermute_b32 v6, v26, v3
	ds_bpermute_b32 v8, v26, v1
	v_add_f32_e32 v2, v2, v5
	v_add_f32_e32 v5, v0, v7
	v_xor_b32_e32 v0, 4, v206
	v_cmp_lt_i32_e32 vcc, v0, v4
	s_waitcnt lgkmcnt(0)
	v_add_f32_e32 v3, v3, v6
	v_add_f32_e32 v6, v1, v8
	v_cndmask_b32_e32 v0, v206, v0, vcc
	v_lshlrev_b32_e32 v27, 2, v0
	ds_bpermute_b32 v0, v27, v2
	ds_bpermute_b32 v1, v27, v3
	ds_bpermute_b32 v7, v27, v5
	ds_bpermute_b32 v8, v27, v6
	v_pk_add_f32 v[16:17], v[72:73], 0 op_sel_hi:[1,0]
	s_waitcnt lgkmcnt(0)
	v_add_f32_e32 v0, v2, v0
	v_add_f32_e32 v1, v3, v1
	v_add_f32_e32 v2, v5, v7
	v_add_f32_e32 v3, v6, v8
	v_pk_add_f32 v[6:7], v[126:127], 0 op_sel_hi:[1,0]
	v_pk_add_f32 v[8:9], v[124:125], 0 op_sel_hi:[1,0]
	v_pk_add_f32 v[6:7], v[6:7], v[114:115]
	v_pk_add_f32 v[8:9], v[8:9], v[112:113]
	v_pk_add_f32 v[6:7], v[6:7], v[110:111]
	v_pk_add_f32 v[8:9], v[8:9], v[108:109]
	v_pk_add_f32 v[6:7], v[6:7], v[98:99]
	v_pk_add_f32 v[8:9], v[8:9], v[96:97]
	v_pk_add_f32 v[6:7], v[6:7], v[86:87]
	v_pk_add_f32 v[8:9], v[8:9], v[84:85]
	v_pk_add_f32 v[6:7], v[6:7], v[66:67]
	v_pk_add_f32 v[8:9], v[8:9], v[64:65]
	v_pk_add_f32 v[6:7], v[6:7], v[122:123]
	v_pk_add_f32 v[8:9], v[8:9], v[120:121]
	v_pk_add_f32 v[6:7], v[6:7], v[134:135]
	v_pk_add_f32 v[8:9], v[8:9], v[132:133]
	ds_bpermute_b32 v10, v21, v8
	ds_bpermute_b32 v12, v21, v6
	ds_bpermute_b32 v13, v21, v7
	ds_bpermute_b32 v11, v21, v9
	v_pk_add_f32 v[16:17], v[16:17], v[56:57]
	s_waitcnt lgkmcnt(0)
	v_add_f32_e32 v8, v8, v10
	v_add_f32_e32 v10, v6, v12
	v_add_f32_e32 v7, v7, v13
	v_add_f32_e32 v9, v9, v11
	ds_bpermute_b32 v11, v26, v8
	ds_bpermute_b32 v13, v26, v10
	ds_bpermute_b32 v14, v26, v7
	ds_bpermute_b32 v12, v26, v9
	v_pk_add_f32 v[16:17], v[16:17], v[52:53]
	s_waitcnt lgkmcnt(0)
	v_add_f32_e32 v8, v8, v11
	v_add_f32_e32 v10, v10, v13
	v_add_f32_e32 v11, v7, v14
	v_add_f32_e32 v9, v9, v12
	ds_bpermute_b32 v12, v27, v8
	ds_bpermute_b32 v14, v27, v10
	ds_bpermute_b32 v15, v27, v11
	v_pk_add_f32 v[16:17], v[16:17], v[48:49]
	ds_bpermute_b32 v13, v27, v9
	s_waitcnt lgkmcnt(0)
	v_add_f32_e32 v8, v8, v12
	v_add_f32_e32 v10, v10, v14
	v_add_f32_e32 v12, v11, v15
	v_pk_add_f32 v[14:15], v[74:75], 0 op_sel_hi:[1,0]
	v_pk_add_f32 v[16:17], v[16:17], v[88:89]
	v_pk_add_f32 v[14:15], v[14:15], v[58:59]
	v_pk_add_f32 v[16:17], v[16:17], v[92:93]
	v_pk_add_f32 v[14:15], v[14:15], v[54:55]
	v_pk_add_f32 v[16:17], v[16:17], v[100:101]
	v_pk_add_f32 v[14:15], v[14:15], v[50:51]
	v_pk_add_f32 v[16:17], v[16:17], v[104:105]
	v_pk_add_f32 v[14:15], v[14:15], v[90:91]
	ds_bpermute_b32 v18, v21, v16
	v_pk_add_f32 v[14:15], v[14:15], v[94:95]
	ds_bpermute_b32 v19, v21, v17
	v_pk_add_f32 v[14:15], v[14:15], v[102:103]
	v_xor_b32_e32 v5, 8, v206
	v_pk_add_f32 v[14:15], v[14:15], v[106:107]
	ds_bpermute_b32 v20, v21, v14
	ds_bpermute_b32 v22, v21, v15
	s_waitcnt lgkmcnt(0)
	v_add_f32_e32 v16, v16, v18
	v_add_f32_e32 v17, v17, v19
	ds_bpermute_b32 v19, v26, v16
	v_add_f32_e32 v18, v14, v20
	v_add_f32_e32 v15, v15, v22
	ds_bpermute_b32 v20, v26, v17
	ds_bpermute_b32 v22, v26, v18
	ds_bpermute_b32 v23, v26, v15
	s_waitcnt lgkmcnt(0)
	v_add_f32_e32 v16, v16, v19
	v_cmp_lt_i32_e32 vcc, v5, v4
	v_add_f32_e32 v17, v17, v20
	v_add_f32_e32 v18, v18, v22
	v_add_f32_e32 v19, v15, v23
	ds_bpermute_b32 v20, v27, v16
	ds_bpermute_b32 v22, v27, v17
	ds_bpermute_b32 v23, v27, v18
	ds_bpermute_b32 v24, v27, v19
	v_cndmask_b32_e32 v4, v206, v5, vcc
	s_waitcnt lgkmcnt(0)
	v_add_f32_e32 v16, v16, v20
	v_add_f32_e32 v17, v17, v22
	v_add_f32_e32 v18, v18, v23
	v_add_f32_e32 v20, v19, v24
	v_pk_add_f32 v[22:23], v[46:47], 0 op_sel_hi:[1,0]
	v_pk_add_f32 v[24:25], v[44:45], 0 op_sel_hi:[1,0]
	v_pk_add_f32 v[22:23], v[22:23], v[42:43]
	v_pk_add_f32 v[24:25], v[24:25], v[40:41]
	v_pk_add_f32 v[22:23], v[22:23], v[38:39]
	v_pk_add_f32 v[24:25], v[24:25], v[36:37]
	v_pk_add_f32 v[22:23], v[22:23], v[34:35]
	v_pk_add_f32 v[24:25], v[24:25], v[32:33]
	v_pk_add_f32 v[22:23], v[22:23], v[62:63]
	v_pk_add_f32 v[24:25], v[24:25], v[60:61]
	v_pk_add_f32 v[22:23], v[22:23], v[70:71]
	v_pk_add_f32 v[24:25], v[24:25], v[68:69]
	v_pk_add_f32 v[22:23], v[22:23], v[78:79]
	v_pk_add_f32 v[24:25], v[24:25], v[76:77]
	v_pk_add_f32 v[22:23], v[22:23], v[82:83]
	v_pk_add_f32 v[24:25], v[24:25], v[80:81]
	ds_bpermute_b32 v28, v21, v24
	ds_bpermute_b32 v29, v21, v25
	ds_bpermute_b32 v30, v21, v22
	ds_bpermute_b32 v32, v21, v23
	v_lshlrev_b32_e32 v31, 2, v4
	s_waitcnt lgkmcnt(0)
	v_add_f32_e32 v24, v24, v28
	v_add_f32_e32 v25, v25, v29
	v_add_f32_e32 v28, v22, v30
	v_add_f32_e32 v23, v23, v32
	ds_bpermute_b32 v29, v26, v24
	ds_bpermute_b32 v30, v26, v25
	ds_bpermute_b32 v32, v26, v28
	ds_bpermute_b32 v26, v26, v23
	v_add_f32_e32 v9, v9, v13
	s_waitcnt lgkmcnt(0)
	v_add_f32_e32 v24, v24, v29
	v_add_f32_e32 v25, v25, v30
	v_add_f32_e32 v28, v28, v32
	v_add_f32_e32 v29, v23, v26
	ds_bpermute_b32 v26, v27, v24
	ds_bpermute_b32 v30, v27, v25
	ds_bpermute_b32 v32, v27, v28
	ds_bpermute_b32 v27, v27, v29
	ds_bpermute_b32 v4, v31, v0
	s_waitcnt lgkmcnt(0)
	v_add_f32_e32 v24, v24, v26
	v_add_f32_e32 v25, v25, v30
	v_add_f32_e32 v26, v28, v32
	v_add_f32_e32 v28, v29, v27
	ds_bpermute_b32 v5, v31, v1
	ds_bpermute_b32 v6, v31, v2
	ds_bpermute_b32 v7, v31, v3
	ds_bpermute_b32 v11, v31, v8
	ds_bpermute_b32 v13, v31, v9
	ds_bpermute_b32 v14, v31, v10
	ds_bpermute_b32 v15, v31, v12
	ds_bpermute_b32 v19, v31, v16
	ds_bpermute_b32 v21, v31, v17
	ds_bpermute_b32 v22, v31, v18
	ds_bpermute_b32 v23, v31, v20
	ds_bpermute_b32 v27, v31, v24
	ds_bpermute_b32 v29, v31, v25
	ds_bpermute_b32 v30, v31, v26
	ds_bpermute_b32 v31, v31, v28
	s_and_saveexec_b64 s[22:23], s[2:3]
	s_cbranch_execz .LBB0_2938
	s_lshl_b32 s5, s4, 1
	s_and_b32 s15, s5, -16
	s_add_i32 s5, s49, s13
	s_lshr_b32 s5, s5, 6
	s_or_b32 s24, s5, s15
	s_ashr_i32 s25, s24, 31
	s_lshl_b64 s[24:25], s[24:25], 11
	s_add_u32 s5, s0, s24
	s_addc_u32 s24, s1, s25
	s_lshl_b32 s4, s4, 8
	s_and_b32 s25, s4, 0x700
	v_add_f32_e32 v0, v0, v4
	s_add_u32 s4, s5, s25
	s_waitcnt lgkmcnt(0)
	v_add_f32_e32 v1, v1, v5
	s_addc_u32 s5, s24, 0
	v_mul_f32_e32 v0, 0x35800000, v0
	v_add_f32_e32 v2, v2, v6
	global_atomic_add_f32 v201, v0, s[4:5]
	v_mul_f32_e32 v0, 0x35800000, v1
	v_add_f32_e32 v3, v3, v7
	global_atomic_add_f32 v201, v0, s[4:5] offset:4
	v_mul_f32_e32 v0, 0x35800000, v2
	global_atomic_add_f32 v201, v0, s[4:5] offset:8
	v_mul_f32_e32 v0, 0x35800000, v3
	global_atomic_add_f32 v201, v0, s[4:5] offset:12
	s_add_i32 s4, s13, s50
	s_lshr_b32 s4, s4, 6
	s_or_b32 s4, s4, s15
	s_ashr_i32 s5, s4, 31
	s_lshl_b64 s[4:5], s[4:5], 11
	s_add_u32 s4, s0, s4
	s_addc_u32 s5, s1, s5
	v_add_f32_e32 v8, v8, v11
	s_add_u32 s4, s4, s25
	v_add_f32_e32 v9, v9, v13
	s_addc_u32 s5, s5, 0
	v_mul_f32_e32 v0, 0x35800000, v8
	v_add_f32_e32 v10, v10, v14
	global_atomic_add_f32 v202, v0, s[4:5]
	v_mul_f32_e32 v0, 0x35800000, v9
	v_add_f32_e32 v12, v12, v15
	global_atomic_add_f32 v201, v0, s[4:5] offset:20
	v_mul_f32_e32 v0, 0x35800000, v10
	global_atomic_add_f32 v202, v0, s[4:5] offset:8
	v_mul_f32_e32 v0, 0x35800000, v12
	global_atomic_add_f32 v201, v0, s[4:5] offset:28
	s_add_i32 s4, s51, s13
	s_lshr_b32 s4, s4, 6
	s_or_b32 s4, s4, s15
	s_ashr_i32 s5, s4, 31
	s_lshl_b64 s[4:5], s[4:5], 11
	s_add_u32 s4, s0, s4
	s_addc_u32 s5, s1, s5
	v_add_f32_e32 v16, v16, v19
	s_add_u32 s4, s4, s25
	v_add_f32_e32 v17, v17, v21
	s_addc_u32 s5, s5, 0
	v_mul_f32_e32 v0, 0x35800000, v16
	v_add_f32_e32 v18, v18, v22
	global_atomic_add_f32 v201, v0, s[4:5]
	v_mul_f32_e32 v0, 0x35800000, v17
	v_add_f32_e32 v20, v20, v23
	global_atomic_add_f32 v201, v0, s[4:5] offset:4
	v_mul_f32_e32 v0, 0x35800000, v18
	global_atomic_add_f32 v201, v0, s[4:5] offset:8
	v_mul_f32_e32 v0, 0x35800000, v20
	s_add_i32 s13, s13, s52
	global_atomic_add_f32 v201, v0, s[4:5] offset:12
	s_lshr_b32 s4, s13, 6
	s_or_b32 s4, s4, s15
	s_ashr_i32 s5, s4, 31
	s_lshl_b64 s[4:5], s[4:5], 11
	s_add_u32 s4, s0, s4
	s_addc_u32 s5, s1, s5
	v_add_f32_e32 v24, v24, v27
	s_add_u32 s4, s4, s25
	v_add_f32_e32 v25, v25, v29
	s_addc_u32 s5, s5, 0
	v_mul_f32_e32 v0, 0x35800000, v24
	v_add_f32_e32 v26, v26, v30
	global_atomic_add_f32 v203, v0, s[4:5]
	v_mul_f32_e32 v0, 0x35800000, v25
	v_add_f32_e32 v28, v28, v31
	global_atomic_add_f32 v201, v0, s[4:5] offset:20
	v_mul_f32_e32 v0, 0x35800000, v26
	global_atomic_add_f32 v203, v0, s[4:5] offset:8
	v_mul_f32_e32 v0, 0x35800000, v28
	global_atomic_add_f32 v201, v0, s[4:5] offset:28
